# baseline (speedup 1.0000x reference)
.LBB1_106:
	v_add_u32_e32 v184, v110, v224
	ds_read_b128 v[6:9], v225 offset:33792
	ds_read_b128 v[10:13], v225 offset:33856
	v_add_u32_e32 v250, v110, v226
	v_add_u32_e32 v185, v110, v227
	ds_read_b32 v20, v184 offset:21504
	ds_read_b32 v21, v250 offset:21504
	ds_read_b32 v22, v185 offset:21504
	ds_read_b128 v[14:17], v225 offset:33920
	v_add_u32_e32 v251, v110, v228
	ds_read_b32 v23, v251 offset:21504
	s_waitcnt lgkmcnt(6)
	v_mov_b32_e32 v0, v6
	s_waitcnt lgkmcnt(5)
	v_mov_b32_e32 v1, v10
	s_waitcnt vmcnt(5)
	v_mul_f32_e32 v2, v182, v6
	s_waitcnt vmcnt(4)
	v_pk_fma_f32 v[0:1], v[182:183], v[0:1], v[2:3] op_sel_hi:[1,1,0]
	s_waitcnt vmcnt(0) lgkmcnt(1)
	v_mul_f32_e32 v181, v186, v14
	v_accvgpr_read_b32 v0, a4
	v_pk_add_f32 v[0:1], v[180:181], v[0:1]
	v_mul_f32_e32 v2, v182, v7
	v_add_f32_e32 v0, v0, v1
	v_mul_f32_e32 v0, 0xbfb8aa3b, v0
	v_exp_f32_e32 v3, v0
	v_mov_b32_e32 v0, v7
	v_mov_b32_e32 v1, v11
	v_mul_f32_e32 v181, v186, v15
	v_pk_fma_f32 v[0:1], v[182:183], v[0:1], v[2:3] op_sel_hi:[1,1,0]
	v_mul_f32_e32 v2, v182, v8
	v_accvgpr_read_b32 v0, a5
	v_pk_add_f32 v[0:1], v[180:181], v[0:1]
	v_mul_f32_e32 v181, v186, v16
	v_add_f32_e32 v0, v0, v1
	v_mul_f32_e32 v0, 0xbfb8aa3b, v0
	v_exp_f32_e32 v0, v0
	v_add_f32_e32 v1, 1.0, v3
	v_rcp_f32_e32 v24, v1
	v_mov_b32_e32 v1, v12
	v_add_f32_e32 v3, 1.0, v0
	v_mov_b32_e32 v0, v8
	v_pk_fma_f32 v[0:1], v[182:183], v[0:1], v[2:3] op_sel_hi:[1,1,0]
	v_mul_f32_e32 v2, v182, v9
	v_accvgpr_read_b32 v0, a6
	v_pk_add_f32 v[0:1], v[180:181], v[0:1]
	v_mul_f32_e32 v181, v186, v17
	v_add_f32_e32 v0, v0, v1
	v_mul_f32_e32 v0, 0xbfb8aa3b, v0
	v_exp_f32_e32 v18, v0
	v_mov_b32_e32 v0, v9
	v_mov_b32_e32 v1, v13
	v_pk_fma_f32 v[0:1], v[182:183], v[0:1], v[2:3] op_sel_hi:[1,1,0]
	v_rcp_f32_e32 v25, v3
	v_accvgpr_read_b32 v0, a7
	v_pk_add_f32 v[0:1], v[180:181], v[0:1]
	s_andn2_b64 vcc, exec, s[28:29]
	v_add_f32_e32 v0, v0, v1
	v_mul_f32_e32 v0, 0xbfb8aa3b, v0
	v_exp_f32_e32 v0, v0
	v_add_f32_e32 v1, 1.0, v18
	v_rcp_f32_e32 v26, v1
	v_mul_f32_e32 v1, v21, v25
	v_add_f32_e32 v0, 1.0, v0
	v_rcp_f32_e32 v27, v0
	v_mul_f32_e32 v2, v22, v26
	v_mul_f32_e32 v0, v20, v24
	v_cvt_pk_f16_f32 v18, v0, v1
	s_waitcnt lgkmcnt(0)
	v_mul_f32_e32 v3, v23, v27
	v_cvt_pk_f16_f32 v19, v2, v3
	v_or_b32_e32 v19, s64, v19
	v_cndmask_b32_e64 v2, 0, 1, s[28:29]
	v_cmp_ne_u32_e64 s[16:17], 1, v2
	s_cbranch_vccnz .LBB1_171
	global_store_dwordx2 v[172:173], v[18:19], off sc0
	s_or_b32 s70, s40, 1
	s_and_saveexec_b64 s[68:69], s[12:13]
	v_mov_b32_e32 v3, s70
	global_store_dword v[174:175], v3, off sc0
	s_mov_b64 exec, s[68:69]
	s_cbranch_execnz .LBB1_109

.Ltg1_go:
	s_nop 1
	v_accvgpr_read_b32 v0, a0
	v_accvgpr_read_b32 v2, a1
	v_accvgpr_read_b32 v1, a2
	v_accvgpr_read_b32 v3, a3
	v_cvt_pk_f16_f32 v1, v1, v3
	v_cvt_pk_f16_f32 v0, v0, v2
	v_add_u32_e32 v182, v111, v207
	v_accvgpr_read_b32 v2, a4
	v_accvgpr_read_b32 v6, a5
	v_accvgpr_read_b32 v3, a6
	v_accvgpr_read_b32 v7, a7
	v_cvt_pk_f16_f32 v3, v3, v7
	v_cvt_pk_f16_f32 v2, v2, v6
	ds_write2_b64 v248, v[0:1], v[2:3] offset0:80 offset1:96
	s_waitcnt lgkmcnt(0)
	s_barrier
	ds_read_b128 v[0:3], v182 offset:12800
	ds_read_b128 v[6:9], v182 offset:12864
	ds_read_b128 v[10:13], v182 offset:12928
	ds_read_b128 v[14:17], v182 offset:12992
	ds_read_b128 v[18:21], v182 offset:13056
	ds_read_b128 v[22:25], v182 offset:13120
	ds_read2st64_b32 v[42:43], v242 offset0:84 offset1:116
	ds_read_b128 v[38:41], v225 offset:33792
	ds_read_b128 v[26:29], v225 offset:33856
	ds_read_b128 v[30:33], v225 offset:33920
	v_or_b32_e32 v36, v110, v227
	v_or_b32_e32 v34, v110, v226
	ds_read2st64_b32 v[44:45], v36 offset0:84 offset1:116
	v_or_b32_e32 v36, v110, v228
	ds_read2st64_b32 v[34:35], v34 offset0:84 offset1:116
	ds_read2st64_b32 v[36:37], v36 offset0:84 offset1:116
	s_waitcnt lgkmcnt(12)
	v_mfma_f32_16x16x32_f16 a[0:3], v[0:3], a[56:59], 0
	s_waitcnt lgkmcnt(11)
	v_mfma_f32_16x16x32_f16 a[0:3], v[6:9], a[60:63], a[0:3]
	s_waitcnt lgkmcnt(10)
	v_mfma_f32_16x16x32_f16 a[0:3], v[10:13], a[64:67], a[0:3]
	s_waitcnt lgkmcnt(9)
	v_mfma_f32_16x16x32_f16 a[0:3], v[14:17], a[68:71], a[0:3]
	s_waitcnt lgkmcnt(8)
	v_mfma_f32_16x16x32_f16 a[0:3], v[18:21], a[72:75], a[0:3]
	s_waitcnt lgkmcnt(7)
	v_mfma_f32_16x16x32_f16 a[0:3], v[22:25], a[76:79], a[0:3]
	s_nop 7
	v_accvgpr_read_b32 v7, a1
	v_accvgpr_read_b32 v9, a0
	v_accvgpr_read_b32 v1, a3
	v_accvgpr_read_b32 v3, a2
	s_waitcnt lgkmcnt(5)
	v_mov_b32_e32 v10, v38
	s_waitcnt lgkmcnt(4)
	v_mov_b32_e32 v11, v26
	s_waitcnt vmcnt(1)
	v_mul_f32_e32 v0, v191, v26
	v_pk_fma_f32 v[10:11], v[190:191], v[10:11], v[0:1] op_sel_hi:[1,1,0]
	s_waitcnt vmcnt(0) lgkmcnt(3)
	v_mul_f32_e32 v8, v192, v30
	v_mov_b32_e32 v11, v186
	v_pk_add_f32 v[8:9], v[10:11], v[8:9]
	v_mov_b32_e32 v26, v39
	v_add_f32_e32 v0, v8, v9
	v_mul_f32_e32 v0, 0x4038aa3b, v0
	v_exp_f32_e32 v2, v0
	v_mul_f32_e32 v0, v191, v27
	v_pk_fma_f32 v[8:9], v[190:191], v[26:27], v[0:1] op_sel_hi:[1,1,0]
	v_mul_f32_e32 v6, v192, v31
	v_mov_b32_e32 v9, v186
	v_pk_add_f32 v[6:7], v[8:9], v[6:7]
	v_mov_b32_e32 v10, v40
	v_add_f32_e32 v0, v6, v7
	v_mul_f32_e32 v0, 0x4038aa3b, v0
	v_exp_f32_e32 v0, v0
	v_mov_b32_e32 v11, v28
	v_add_f32_e32 v2, 1.0, v2
	v_rcp_f32_e32 v6, v2
	v_add_f32_e32 v0, 1.0, v0
	v_rcp_f32_e32 v7, v0
	v_mul_f32_e32 v0, v191, v28
	v_pk_fma_f32 v[10:11], v[190:191], v[10:11], v[0:1] op_sel_hi:[1,1,0]
	v_mul_f32_e32 v2, v192, v32
	v_mov_b32_e32 v11, v186
	v_pk_add_f32 v[2:3], v[10:11], v[2:3]
	v_mov_b32_e32 v28, v41
	v_add_f32_e32 v0, v2, v3
	v_mul_f32_e32 v2, v191, v29
	v_mul_f32_e32 v0, 0x4038aa3b, v0
	v_pk_fma_f32 v[2:3], v[190:191], v[28:29], v[2:3] op_sel_hi:[1,1,0]
	v_exp_f32_e32 v10, v0
	v_mul_f32_e32 v0, v192, v33
	v_mov_b32_e32 v3, v186
	v_pk_add_f32 v[0:1], v[2:3], v[0:1]
	v_add_f32_e32 v2, 1.0, v10
	v_add_f32_e32 v0, v0, v1
	v_mul_f32_e32 v0, 0x4038aa3b, v0
	v_exp_f32_e32 v3, v0
	v_rcp_f32_e32 v2, v2
	s_waitcnt lgkmcnt(1)
	v_mov_b32_e32 v9, v34
	v_mov_b32_e32 v34, v43
	v_add_f32_e32 v3, 1.0, v3
	v_rcp_f32_e32 v3, v3
	v_pk_fma_f32 v[6:7], v[6:7], 2.0, 1.0 op_sel_hi:[1,0,0] neg_lo:[1,0,0] neg_hi:[1,0,0]
	v_pk_add_f32 v[0:1], v[34:35], 1.0 op_sel_hi:[1,0] neg_lo:[1,0] neg_hi:[1,0]
	v_mov_b32_e32 v8, v42
	v_pk_mul_f32 v[0:1], v[0:1], v[6:7]
	s_and_b64 vcc, exec, s[16:17]
	v_pk_fma_f32 v[8:9], v[8:9], v[34:35], v[0:1]
	v_pk_fma_f32 v[0:1], v[2:3], 2.0, 1.0 op_sel_hi:[1,0,0] neg_lo:[1,0,0] neg_hi:[1,0,0]
	s_waitcnt lgkmcnt(0)
	v_mov_b32_e32 v3, v36
	v_mov_b32_e32 v36, v45
	v_pk_add_f32 v[10:11], v[36:37], 1.0 op_sel_hi:[1,0] neg_lo:[1,0] neg_hi:[1,0]
	v_mov_b32_e32 v2, v44
	v_pk_mul_f32 v[0:1], v[10:11], v[0:1]
	v_cvt_pk_f16_f32 v6, v8, v9
	v_pk_fma_f32 v[10:11], v[2:3], v[36:37], v[0:1]
	s_nop 0
	v_cvt_pk_f16_f32 v7, v10, v11
	v_mov_b32_e32 v2, v6
	v_or_b32_e32 v3, s64, v7
	s_cbranch_vccnz .LBB1_125
	s_mov_b64 s[36:37], 0
	global_store_dwordx2 v[178:179], v[2:3], off sc0
	s_or_b32 s70, s40, 2
	s_and_saveexec_b64 s[68:69], s[12:13]
	v_mov_b32_e32 v0, s70
	global_store_dword v[174:175], v0, off sc0
	s_mov_b64 exec, s[68:69]

.Ltg2_go:
	s_nop 1
	v_accvgpr_read_b32 v30, a128
	v_accvgpr_read_b32 v32, a129
	v_accvgpr_read_b32 v31, a130
	v_accvgpr_read_b32 v33, a131
	v_cvt_pk_f16_f32 v31, v31, v33
	v_cvt_pk_f16_f32 v30, v30, v32
	v_accvgpr_read_b32 v32, a132
	v_accvgpr_read_b32 v34, a133
	v_accvgpr_read_b32 v33, a134
	v_accvgpr_read_b32 v35, a135
	v_cvt_pk_f16_f32 v33, v33, v35
	v_cvt_pk_f16_f32 v32, v32, v34
	ds_write2_b64 v221, v[30:31], v[32:33] offset0:32 offset1:64
	s_waitcnt lgkmcnt(0)
	s_barrier
	ds_read_b128 v[34:37], v249
	ds_read_b128 v[38:41], v249 offset:64
	ds_read_b128 v[42:45], v249 offset:256
	ds_read_b128 v[46:49], v249 offset:320
	ds_read_b128 v[50:53], v249 offset:512
	ds_read_b128 v[30:33], v249 offset:576
	ds_read2st64_b32 v[56:57], v184 offset0:100 offset1:101
	ds_read2st64_b32 v[54:55], v184 offset0:102 offset1:103
	s_waitcnt lgkmcnt(7)
	v_mfma_f32_16x16x32_f16 a[4:7], v[34:37], v[0:3], a[4:7]
	s_waitcnt lgkmcnt(6)
	v_mfma_f32_16x16x32_f16 a[4:7], v[38:41], v[64:67], a[4:7]
	s_waitcnt lgkmcnt(5)
	v_mfma_f32_16x16x32_f16 a[4:7], v[42:45], v[68:71], a[4:7]
	s_waitcnt lgkmcnt(4)
	v_mfma_f32_16x16x32_f16 a[4:7], v[46:49], v[72:75], a[4:7]
	s_waitcnt lgkmcnt(3)
	v_mfma_f32_16x16x32_f16 a[4:7], v[50:53], v[78:81], a[4:7]
	s_waitcnt lgkmcnt(2)
	v_mfma_f32_16x16x32_f16 a[4:7], v[30:33], v[82:85], a[4:7]
	s_nop 7
	v_accvgpr_read_b32 v0, a4
	s_waitcnt vmcnt(0)
	v_add_f32_e32 v0, v180, v0
	v_accvgpr_read_b32 v1, a5
	v_mul_f32_e32 v0, 0xbfb8aa3b, v0
	v_add_f32_e32 v1, v180, v1
	v_exp_f32_e32 v0, v0
	v_mul_f32_e32 v1, 0xbfb8aa3b, v1
	v_exp_f32_e32 v1, v1
	v_accvgpr_read_b32 v2, a7
	v_add_f32_e32 v0, 1.0, v0
	v_rcp_f32_e32 v186, v0
	v_add_f32_e32 v0, 1.0, v1
	v_accvgpr_read_b32 v1, a6
	v_add_f32_e32 v1, v180, v1
	v_mul_f32_e32 v1, 0xbfb8aa3b, v1
	v_add_f32_e32 v2, v180, v2
	v_exp_f32_e32 v1, v1
	v_mul_f32_e32 v2, 0xbfb8aa3b, v2
	v_exp_f32_e32 v2, v2
	v_rcp_f32_e32 v252, v0
	v_add_f32_e32 v0, 1.0, v1
	v_rcp_f32_e32 v253, v0
	v_add_f32_e32 v0, 1.0, v2
	v_rcp_f32_e32 v254, v0
	s_waitcnt lgkmcnt(1)
	v_mul_f32_e32 v0, v56, v186
	v_mul_f32_e32 v1, v57, v252
	s_waitcnt lgkmcnt(0)
	v_mul_f32_e32 v2, v54, v253
	v_mul_f32_e32 v3, v55, v254
	v_cvt_pk_f16_f32 v181, v2, v3
	s_and_b64 vcc, exec, s[16:17]
	v_cvt_pk_f16_f32 v180, v0, v1
	s_cbranch_vccnz .LBB1_143
	s_mov_b64 s[36:37], 0
	global_store_dwordx2 v[172:173], v[180:181], off sc0
	s_or_b32 s70, s40, 3
	s_and_saveexec_b64 s[68:69], s[12:13]
	v_mov_b32_e32 v3, s70
	global_store_dword v[174:175], v3, off sc0
	s_mov_b64 exec, s[68:69]

.Ltg3_go:
	s_nop 1
	v_accvgpr_read_b32 v0, a4
	v_accvgpr_read_b32 v2, a5
	v_accvgpr_read_b32 v1, a6
	v_accvgpr_read_b32 v3, a7
	v_cvt_pk_f16_f32 v1, v1, v3
	v_cvt_pk_f16_f32 v0, v0, v2
	v_accvgpr_read_b32 v2, a128
	v_accvgpr_read_b32 v6, a129
	v_accvgpr_read_b32 v3, a130
	v_accvgpr_read_b32 v7, a131
	v_cvt_pk_f16_f32 v3, v3, v7
	v_cvt_pk_f16_f32 v2, v2, v6
	ds_write2_b64 v221, v[0:1], v[2:3] offset0:48 offset1:80
	s_waitcnt lgkmcnt(0)
	s_barrier
	ds_read_b128 v[0:3], v182 offset:12800
	ds_read_b128 v[6:9], v182 offset:12864
	ds_read_b128 v[10:13], v249 offset:384
	ds_read_b128 v[14:17], v249 offset:448
	ds_read_b128 v[18:21], v249 offset:640
	ds_read_b128 v[22:25], v249 offset:704
	ds_read2st64_b32 v[26:27], v242 offset0:100 offset1:101
	ds_read2st64_b32 v[28:29], v242 offset0:116 offset1:117
	ds_read2st64_b32 v[30:31], v242 offset0:118 offset1:119
	ds_read2st64_b32 v[32:33], v242 offset0:102 offset1:103
	s_waitcnt lgkmcnt(9)
	v_mfma_f32_16x16x32_f16 a[0:3], v[0:3], a[88:91], a[0:3]
	s_waitcnt lgkmcnt(8)
	v_mfma_f32_16x16x32_f16 a[0:3], v[6:9], a[92:95], a[0:3]
	s_waitcnt lgkmcnt(7)
	v_mfma_f32_16x16x32_f16 a[0:3], v[10:13], a[104:107], a[0:3]
	s_waitcnt lgkmcnt(6)
	v_mfma_f32_16x16x32_f16 a[0:3], v[14:17], a[108:111], a[0:3]
	s_waitcnt lgkmcnt(5)
	v_mfma_f32_16x16x32_f16 a[0:3], v[18:21], a[120:123], a[0:3]
	s_waitcnt lgkmcnt(4)
	v_mfma_f32_16x16x32_f16 a[0:3], v[22:25], a[124:127], a[0:3]
	s_nop 7
	v_accvgpr_read_b32 v0, a0
	v_accvgpr_read_b32 v1, a1
	s_waitcnt vmcnt(0)
	v_add_f32_e32 v0, v180, v0
	v_add_f32_e32 v1, v180, v1
	v_mul_f32_e32 v0, 0x4038aa3b, v0
	v_mul_f32_e32 v1, 0x4038aa3b, v1
	v_exp_f32_e32 v0, v0
	v_exp_f32_e32 v1, v1
	s_waitcnt lgkmcnt(2)
	v_pk_add_f32 v[2:3], v[28:29], 1.0 op_sel_hi:[1,0] neg_lo:[1,0] neg_hi:[1,0]
	s_and_b64 vcc, exec, s[16:17]
	v_add_f32_e32 v0, 1.0, v0
	v_add_f32_e32 v1, 1.0, v1
	v_rcp_f32_e32 v0, v0
	v_rcp_f32_e32 v1, v1
	s_nop 0
	v_pk_fma_f32 v[0:1], v[0:1], 2.0, 1.0 op_sel_hi:[1,0,0] neg_lo:[1,0,0] neg_hi:[1,0,0]
	s_nop 0
	v_pk_mul_f32 v[0:1], v[2:3], v[0:1]
	s_waitcnt lgkmcnt(1)
	v_pk_add_f32 v[2:3], v[30:31], 1.0 op_sel_hi:[1,0] neg_lo:[1,0] neg_hi:[1,0]
	v_pk_fma_f32 v[6:7], v[26:27], v[28:29], v[0:1]
	v_accvgpr_read_b32 v0, a2
	v_accvgpr_read_b32 v1, a3
	v_add_f32_e32 v0, v180, v0
	v_add_f32_e32 v1, v180, v1
	v_mul_f32_e32 v0, 0x4038aa3b, v0
	v_mul_f32_e32 v1, 0x4038aa3b, v1
	v_exp_f32_e32 v0, v0
	v_exp_f32_e32 v1, v1
	v_cvt_pk_f16_f32 v10, v6, v7
	v_add_f32_e32 v0, 1.0, v0
	v_add_f32_e32 v1, 1.0, v1
	v_rcp_f32_e32 v0, v0
	v_rcp_f32_e32 v1, v1
	s_nop 0
	v_pk_fma_f32 v[0:1], v[0:1], 2.0, 1.0 op_sel_hi:[1,0,0] neg_lo:[1,0,0] neg_hi:[1,0,0]
	s_nop 0
	v_pk_mul_f32 v[0:1], v[2:3], v[0:1]
	s_waitcnt lgkmcnt(0)
	v_pk_fma_f32 v[8:9], v[32:33], v[30:31], v[0:1]
	s_nop 0
	v_cvt_pk_f16_f32 v11, v8, v9
	s_cbranch_vccnz .LBB1_172
	global_store_dwordx2 v[178:179], v[10:11], off sc0
	s_add_i32 s70, s40, 4
	s_and_saveexec_b64 s[68:69], s[12:13]
	v_mov_b32_e32 v3, s70
	global_store_dword v[174:175], v3, off sc0
	s_mov_b64 exec, s[68:69]
	s_cbranch_execnz .LBB1_162
